# window attention unit prologue: the first tile's eight K-fragment LDS reads issued together into dead registers and waited by count instead of read-wait-MFMA one at a time
# baseline (speedup 1.0000x reference)
.LBB0_1966:
	v_lshrrev_b32_e32 v2, 5, v179
	v_lshlrev_b32_e32 v3, 7, v185
	v_bitop3_b32 v4, v2, v186, 1 bitop3:0x78
	v_lshlrev_b32_e32 v88, 3, v185
	v_lshlrev_b32_e32 v187, 2, v2
	v_and_b32_e32 v2, 0xf80, v3
	v_and_b32_e32 v6, 0x60, v88
	v_lshl_or_b32 v7, v4, 4, v2
	v_or_b32_e32 v190, v7, v6
	v_add_u32_e32 v194, 0, v190
	ds_read_b128 v[2:5], v194
	v_bitop3_b32 v191, v7, 32, v6 bitop3:0x36
	v_add_u32_e32 v195, 0, v191
	v_bitop3_b32 v192, v7, 64, v6 bitop3:0x36
	v_add_u32_e32 v196, 0, v192
	s_movk_i32 s2, 0x60
	v_bitop3_b32 v193, v7, s2, v88 bitop3:0x34
	v_add_u32_e32 v197, 0, v193
	s_cmp_lt_i32 s87, 1
	ds_read_b128 v[8:11], v194 offset:4096
	ds_read_b128 v[12:15], v195
	ds_read_b128 v[16:19], v195 offset:4096
	ds_read_b128 v[20:23], v196
	ds_read_b128 v[24:27], v196 offset:4096
	ds_read_b128 v[28:31], v197
	ds_read_b128 v[32:35], v197 offset:4096
	s_waitcnt vmcnt(0) lgkmcnt(7)
	v_mfma_f32_32x32x16_bf16 v[50:65], v[2:5], v[82:85], 0
	s_waitcnt lgkmcnt(6)
	v_mfma_f32_32x32x16_bf16 v[66:81], v[8:11], v[82:85], 0
	s_waitcnt lgkmcnt(5)
	v_mfma_f32_32x32x16_bf16 v[50:65], v[12:15], v[140:143], v[50:65]
	s_waitcnt lgkmcnt(4)
	v_mfma_f32_32x32x16_bf16 v[66:81], v[16:19], v[140:143], v[66:81]
	s_waitcnt lgkmcnt(3)
	v_mfma_f32_32x32x16_bf16 v[50:65], v[20:23], v[136:139], v[50:65]
	s_waitcnt lgkmcnt(2)
	v_mfma_f32_32x32x16_bf16 v[66:81], v[24:27], v[136:139], v[66:81]
	s_waitcnt lgkmcnt(1)
	v_mfma_f32_32x32x16_bf16 v[50:65], v[28:31], v[132:135], v[50:65]
	s_waitcnt lgkmcnt(0)
	v_mfma_f32_32x32x16_bf16 v[66:81], v[32:35], v[132:135], v[66:81]
	s_cbranch_scc1 .LBB0_1971
	s_sub_i32 s2, s86, s89
	s_add_i32 s2, s2, 63
	s_cmpk_gt_i32 s2, 0x80
	s_cselect_b64 s[38:39], -1, 0
	s_and_b64 vcc, exec, s[38:39]
	s_cbranch_vccnz .LBB0_1969
	s_sub_i32 s2, s89, s86
	s_add_i32 s2, s2, 31
	s_cmpk_gt_i32 s2, 0x80
	s_cselect_b64 s[38:39], -1, 0
